# hcat phase: the gain vector is loaded once (4 x 16 B per lane) instead of twelve single loads each followed by vmcnt(0) that also drained the output stores
# baseline (speedup 1.0000x reference)
.Lada_wait_skip:
	s_barrier
	s_load_dwordx2 s[28:29], s[12:13], 0x28
	s_ashr_i32 s39, s37, 7
	s_mul_i32 s40, s39, 0x6000
	v_lshlrev_b32_e32 v144, 2, v186
	v_add_u32_e32 v145, 0x1000, v144
	s_add_u32 s60, s14, s40
	s_addc_u32 s61, s15, 0
	s_add_u32 s76, s14, 0xc000
	s_addc_u32 s77, s15, 0
	s_add_u32 s62, s60, 0x12000
	s_addc_u32 s63, s61, 0
	s_add_u32 s78, s76, 0x12000
	s_addc_u32 s79, s77, 0
	s_add_u32 s64, s62, 0x12000
	s_addc_u32 s65, s63, 0
	s_add_u32 s80, s78, 0x12000
	s_addc_u32 s81, s79, 0
	s_add_u32 s66, s64, 0x12000
	s_addc_u32 s67, s65, 0
	s_add_u32 s82, s80, 0x12000
	s_addc_u32 s83, s81, 0
	s_add_u32 s68, s66, 0x12000
	s_addc_u32 s69, s67, 0
	s_add_u32 s84, s82, 0x12000
	s_addc_u32 s85, s83, 0
	s_add_u32 s70, s68, 0x12000
	s_addc_u32 s71, s69, 0
	s_add_u32 s86, s84, 0x12000
	s_addc_u32 s87, s85, 0
	s_add_u32 s72, s70, 0x12000
	s_addc_u32 s73, s71, 0
	s_add_u32 s88, s86, 0x12000
	s_addc_u32 s89, s87, 0
	s_add_u32 s74, s72, 0x12000
	s_addc_u32 s75, s73, 0
	s_add_u32 s90, s88, 0x12000
	s_addc_u32 s91, s89, 0
	s_waitcnt lgkmcnt(0)
	global_load_dword v146, v144, s[28:29]
	global_load_dword v147, v144, s[28:29] offset:2048
	global_load_dword v150, v145, s[28:29]
	global_load_dword v161, v145, s[28:29] offset:2048
	global_load_dword v163, v144, s[60:61]
	global_load_dword v165, v144, s[60:61] offset:2048
	global_load_dword v174, v145, s[60:61]
	global_load_dword v175, v145, s[60:61] offset:2048
	global_load_dword v176, v144, s[62:63]
	global_load_dword v177, v144, s[62:63] offset:2048
	global_load_dword v178, v145, s[62:63]
	global_load_dword v179, v145, s[62:63] offset:2048
	global_load_dword v180, v144, s[64:65]
	global_load_dword v182, v144, s[64:65] offset:2048
	global_load_dword v184, v145, s[64:65]
	global_load_dword v201, v145, s[64:65] offset:2048
	global_load_dword v202, v144, s[66:67]
	global_load_dword v203, v144, s[66:67] offset:2048
	global_load_dword v204, v145, s[66:67]
	global_load_dword v205, v145, s[66:67] offset:2048
	global_load_dword v206, v144, s[68:69]
	global_load_dword v207, v144, s[68:69] offset:2048
	global_load_dword v208, v145, s[68:69]
	global_load_dword v209, v145, s[68:69] offset:2048
	global_load_dword v210, v144, s[70:71]
	global_load_dword v211, v144, s[70:71] offset:2048
	global_load_dword v212, v145, s[70:71]
	global_load_dword v213, v145, s[70:71] offset:2048
	global_load_dword v214, v144, s[72:73]
	global_load_dword v215, v144, s[72:73] offset:2048
	global_load_dword v216, v145, s[72:73]
	global_load_dword v217, v145, s[72:73] offset:2048
	global_load_dword v218, v144, s[74:75]
	global_load_dword v219, v144, s[74:75] offset:2048
	global_load_dword v220, v145, s[74:75]
	global_load_dword v221, v145, s[74:75] offset:2048
	global_load_dword v222, v144, s[76:77]
	global_load_dword v223, v144, s[76:77] offset:2048
	global_load_dword v224, v145, s[76:77]
	global_load_dword v225, v145, s[76:77] offset:2048
	global_load_dword v226, v144, s[78:79]
	global_load_dword v227, v144, s[78:79] offset:2048
	global_load_dword v228, v145, s[78:79]
	global_load_dword v229, v145, s[78:79] offset:2048
	global_load_dword v230, v144, s[80:81]
	global_load_dword v231, v144, s[80:81] offset:2048
	global_load_dword v232, v145, s[80:81]
	global_load_dword v233, v145, s[80:81] offset:2048
	global_load_dword v234, v144, s[82:83]
	global_load_dword v236, v144, s[82:83] offset:2048
	global_load_dword v237, v145, s[82:83]
	global_load_dword v238, v145, s[82:83] offset:2048
	global_load_dword v239, v144, s[84:85]
	global_load_dword v240, v144, s[84:85] offset:2048
	global_load_dword v241, v145, s[84:85]
	global_load_dword v242, v145, s[84:85] offset:2048
	global_load_dword v243, v144, s[86:87]
	global_load_dword v244, v144, s[86:87] offset:2048
	global_load_dword v245, v145, s[86:87]
	global_load_dword v246, v145, s[86:87] offset:2048
	global_load_dword v247, v144, s[88:89]
	global_load_dword v248, v144, s[88:89] offset:2048
	global_load_dword v249, v145, s[88:89]
	global_load_dword v250, v145, s[88:89] offset:2048
	global_load_dword v251, v144, s[90:91]
	global_load_dword v252, v144, s[90:91] offset:2048
	global_load_dword v253, v145, s[90:91]
	global_load_dword v254, v145, s[90:91] offset:2048
	s_waitcnt vmcnt(0)
	v_add_f32_e32 v163, v146, v163
	v_add_f32_e32 v222, v146, v222
	v_add_f32_e32 v165, v147, v165
	v_add_f32_e32 v223, v147, v223
	v_add_f32_e32 v174, v150, v174
	v_add_f32_e32 v224, v150, v224
	v_add_f32_e32 v175, v161, v175
	v_add_f32_e32 v225, v161, v225
	v_add_f32_e32 v163, v163, v176
	v_add_f32_e32 v222, v222, v226
	v_add_f32_e32 v165, v165, v177
	v_add_f32_e32 v223, v223, v227
	v_add_f32_e32 v174, v174, v178
	v_add_f32_e32 v224, v224, v228
	v_add_f32_e32 v175, v175, v179
	v_add_f32_e32 v225, v225, v229
	v_add_f32_e32 v163, v163, v180
	v_add_f32_e32 v222, v222, v230
	v_add_f32_e32 v165, v165, v182
	v_add_f32_e32 v223, v223, v231
	v_add_f32_e32 v174, v174, v184
	v_add_f32_e32 v224, v224, v232
	v_add_f32_e32 v175, v175, v201
	v_add_f32_e32 v225, v225, v233
	v_add_f32_e32 v163, v163, v202
	v_add_f32_e32 v222, v222, v234
	v_add_f32_e32 v165, v165, v203
	v_add_f32_e32 v223, v223, v236
	v_add_f32_e32 v174, v174, v204
	v_add_f32_e32 v224, v224, v237
	v_add_f32_e32 v175, v175, v205
	v_add_f32_e32 v225, v225, v238
	v_add_f32_e32 v163, v163, v206
	v_add_f32_e32 v222, v222, v239
	v_add_f32_e32 v165, v165, v207
	v_add_f32_e32 v223, v223, v240
	v_add_f32_e32 v174, v174, v208
	v_add_f32_e32 v224, v224, v241
	v_add_f32_e32 v175, v175, v209
	v_add_f32_e32 v225, v225, v242
	v_add_f32_e32 v163, v163, v210
	v_add_f32_e32 v222, v222, v243
	v_add_f32_e32 v165, v165, v211
	v_add_f32_e32 v223, v223, v244
	v_add_f32_e32 v174, v174, v212
	v_add_f32_e32 v224, v224, v245
	v_add_f32_e32 v175, v175, v213
	v_add_f32_e32 v225, v225, v246
	v_add_f32_e32 v163, v163, v214
	v_add_f32_e32 v222, v222, v247
	v_add_f32_e32 v165, v165, v215
	v_add_f32_e32 v223, v223, v248
	v_add_f32_e32 v174, v174, v216
	v_add_f32_e32 v224, v224, v249
	v_add_f32_e32 v175, v175, v217
	v_add_f32_e32 v225, v225, v250
	v_add_f32_e32 v163, v163, v218
	v_add_f32_e32 v222, v222, v251
	v_add_f32_e32 v165, v165, v219
	v_add_f32_e32 v223, v223, v252
	v_add_f32_e32 v174, v174, v220
	v_add_f32_e32 v224, v224, v253
	v_add_f32_e32 v175, v175, v221
	v_add_f32_e32 v225, v225, v254
	ds_write_b32 v144, v163
	ds_write_b32 v144, v222 offset:8192
	ds_write_b32 v144, v165 offset:2048
	ds_write_b32 v144, v223 offset:10240
	ds_write_b32 v144, v174 offset:4096
	ds_write_b32 v144, v224 offset:12288
	ds_write_b32 v144, v175 offset:6144
	ds_write_b32 v144, v225 offset:14336
	s_waitcnt lgkmcnt(0)
	global_load_dwordx4 v[240:243], v[156:157], off
	global_load_dwordx4 v[244:247], v[156:157], off offset:1024
	global_load_dwordx4 v[248:251], v[156:157], off offset:2048
	global_load_dwordx4 v[252:255], v[156:157], off offset:3072
	s_waitcnt vmcnt(35)
	v_mov_b32_e32 v146, v129
	s_waitcnt vmcnt(34)
	v_mov_b32_e32 v147, v125
	v_mov_b32_e32 v144, v128
	v_mov_b32_e32 v145, v124
	v_pk_mul_f32 v[146:147], v[146:147], v[146:147]
	s_waitcnt vmcnt(33)
	v_mov_b32_e32 v174, v97
	v_pk_fma_f32 v[144:145], v[144:145], v[144:145], v[146:147]
	v_mov_b32_e32 v146, v130
	v_mov_b32_e32 v147, v126
	v_pk_fma_f32 v[144:145], v[146:147], v[146:147], v[144:145]
	v_mov_b32_e32 v146, v131
	v_mov_b32_e32 v147, v127
	s_waitcnt vmcnt(32)
	v_mov_b32_e32 v175, v85
	v_pk_fma_f32 v[144:145], v[146:147], v[146:147], v[144:145]
	v_mov_b32_e32 v146, v96
	v_mov_b32_e32 v147, v84
	v_pk_mul_f32 v[174:175], v[174:175], v[174:175]
	s_waitcnt vmcnt(31)
	v_mov_b32_e32 v176, v133
	v_pk_fma_f32 v[146:147], v[146:147], v[146:147], v[174:175]
	v_mov_b32_e32 v174, v98
	v_mov_b32_e32 v175, v86
	v_pk_fma_f32 v[146:147], v[174:175], v[174:175], v[146:147]
	v_mov_b32_e32 v174, v99
	v_mov_b32_e32 v175, v87
	s_waitcnt vmcnt(30)
	v_mov_b32_e32 v177, v113
	v_pk_fma_f32 v[146:147], v[174:175], v[174:175], v[146:147]
	v_mov_b32_e32 v174, v132
	v_mov_b32_e32 v175, v112
	v_pk_mul_f32 v[176:177], v[176:177], v[176:177]
	s_waitcnt vmcnt(29)
	v_mov_b32_e32 v178, v101
	v_pk_fma_f32 v[174:175], v[174:175], v[174:175], v[176:177]
	v_mov_b32_e32 v176, v134
	v_mov_b32_e32 v177, v114
	v_pk_fma_f32 v[174:175], v[176:177], v[176:177], v[174:175]
	v_mov_b32_e32 v176, v135
	v_mov_b32_e32 v177, v115
	s_waitcnt vmcnt(28)
	v_mov_b32_e32 v179, v89
	v_pk_fma_f32 v[174:175], v[176:177], v[176:177], v[174:175]
	v_mov_b32_e32 v176, v100
	v_mov_b32_e32 v177, v88
	v_pk_mul_f32 v[178:179], v[178:179], v[178:179]
	s_waitcnt vmcnt(23)
	v_mov_b32_e32 v202, v141
	v_pk_fma_f32 v[176:177], v[176:177], v[176:177], v[178:179]
	v_mov_b32_e32 v178, v102
	v_mov_b32_e32 v179, v90
	v_pk_fma_f32 v[176:177], v[178:179], v[178:179], v[176:177]
	v_mov_b32_e32 v178, v103
	v_mov_b32_e32 v179, v91
	v_pk_fma_f32 v[176:177], v[178:179], v[178:179], v[176:177]
	v_mov_b32_e32 v178, v174
	v_mov_b32_e32 v179, v144
	v_mov_b32_e32 v144, v175
	v_pk_add_f32 v[144:145], v[178:179], v[144:145]
	v_mov_b32_e32 v174, v176
	v_mov_b32_e32 v175, v146
	v_mov_b32_e32 v146, v177
	v_mov_b32_e32 v176, v137
	v_mov_b32_e32 v177, v117
	v_pk_add_f32 v[144:145], v[144:145], v[174:175]
	v_mov_b32_e32 v174, v136
	v_mov_b32_e32 v175, v116
	v_pk_mul_f32 v[176:177], v[176:177], v[176:177]
	v_mov_b32_e32 v178, v105
	v_pk_fma_f32 v[174:175], v[174:175], v[174:175], v[176:177]
	v_mov_b32_e32 v176, v138
	v_mov_b32_e32 v177, v118
	v_pk_fma_f32 v[174:175], v[176:177], v[176:177], v[174:175]
	v_mov_b32_e32 v176, v139
	v_mov_b32_e32 v177, v119
	v_mov_b32_e32 v179, v93
	v_pk_fma_f32 v[174:175], v[176:177], v[176:177], v[174:175]
	v_mov_b32_e32 v176, v104
	v_mov_b32_e32 v177, v92
	v_pk_mul_f32 v[178:179], v[178:179], v[178:179]
	s_waitcnt vmcnt(22)
	v_mov_b32_e32 v203, v121
	v_pk_fma_f32 v[176:177], v[176:177], v[176:177], v[178:179]
	v_mov_b32_e32 v178, v106
	v_mov_b32_e32 v179, v94
	v_pk_fma_f32 v[176:177], v[178:179], v[178:179], v[176:177]
	v_mov_b32_e32 v178, v107
	v_mov_b32_e32 v179, v95
	v_pk_fma_f32 v[176:177], v[178:179], v[178:179], v[176:177]
	v_mov_b32_e32 v178, v140
	v_mov_b32_e32 v179, v120
	v_pk_mul_f32 v[202:203], v[202:203], v[202:203]
	s_waitcnt lgkmcnt(0)
	v_pk_fma_f32 v[178:179], v[178:179], v[178:179], v[202:203]
	v_mov_b32_e32 v202, v142
	v_mov_b32_e32 v203, v122
	v_pk_fma_f32 v[178:179], v[202:203], v[202:203], v[178:179]
	v_mov_b32_e32 v202, v143
	v_mov_b32_e32 v203, v123
	s_barrier
	v_pk_fma_f32 v[178:179], v[202:203], v[202:203], v[178:179]
	s_nop 0
	v_pk_add_f32 v[144:145], v[144:145], v[146:147]
	ds_bpermute_b32 v147, v189, v145
	ds_bpermute_b32 v146, v189, v144
	s_waitcnt vmcnt(22)
	v_mov_b32_e32 v208, v109
	s_waitcnt vmcnt(21)
	v_mov_b32_e32 v209, v81
	v_mov_b32_e32 v206, v108
	v_mov_b32_e32 v207, v80
	s_waitcnt lgkmcnt(0)
	v_pk_add_f32 v[144:145], v[144:145], v[146:147]
	ds_bpermute_b32 v147, v190, v145
	ds_bpermute_b32 v146, v190, v144
	v_pk_mul_f32 v[208:209], v[208:209], v[208:209]
	v_lshlrev_b64 v[168:169], 11, v[168:169]
	v_pk_fma_f32 v[206:207], v[206:207], v[206:207], v[208:209]
	v_mov_b32_e32 v208, v110
	s_waitcnt lgkmcnt(0)
	v_pk_add_f32 v[144:145], v[144:145], v[146:147]
	ds_bpermute_b32 v147, v191, v145
	ds_bpermute_b32 v146, v191, v144
	v_mov_b32_e32 v209, v82
	v_pk_fma_f32 v[206:207], v[208:209], v[208:209], v[206:207]
	v_mov_b32_e32 v208, v111
	v_mov_b32_e32 v209, v83
	v_pk_fma_f32 v[206:207], v[208:209], v[208:209], v[206:207]
	v_mov_b32_e32 v208, v178
	v_mov_b32_e32 v209, v174
	v_mov_b32_e32 v174, v179
	v_pk_add_f32 v[174:175], v[208:209], v[174:175]
	v_mov_b32_e32 v178, v206
	v_mov_b32_e32 v179, v176
	v_pk_add_f32 v[174:175], v[174:175], v[178:179]
	v_mov_b32_e32 v176, v207
	s_waitcnt lgkmcnt(0)
	v_pk_add_f32 v[144:145], v[144:145], v[146:147]
	v_pk_add_f32 v[174:175], v[174:175], v[176:177]
	ds_bpermute_b32 v147, v192, v145
	ds_bpermute_b32 v146, v192, v144
	ds_bpermute_b32 v177, v189, v175
	ds_bpermute_b32 v176, v189, v174
	ds_read_b128 v[206:209], v196 offset:4096
	v_lshlrev_b64 v[170:171], 11, v[170:171]
	s_waitcnt lgkmcnt(3)
	v_pk_add_f32 v[144:145], v[144:145], v[146:147]
	ds_bpermute_b32 v147, v193, v145
	s_waitcnt lgkmcnt(2)
	v_pk_add_f32 v[174:175], v[174:175], v[176:177]
	ds_bpermute_b32 v146, v193, v144
	ds_bpermute_b32 v177, v190, v175
	ds_bpermute_b32 v176, v190, v174
	v_mov_b32_e32 v165, v151
	s_waitcnt lgkmcnt(2)
	v_pk_add_f32 v[144:145], v[144:145], v[146:147]
	ds_bpermute_b32 v147, v194, v145
	s_waitcnt lgkmcnt(1)
	v_pk_add_f32 v[176:177], v[174:175], v[176:177]
	ds_bpermute_b32 v146, v194, v144
	ds_bpermute_b32 v179, v191, v177
	ds_bpermute_b32 v178, v191, v176
	v_mov_b64_e32 v[174:175], s[22:23]
	s_waitcnt lgkmcnt(2)
	v_pk_add_f32 v[144:145], v[144:145], v[146:147]
	s_nop 0
	v_pk_fma_f32 v[144:145], v[144:145], s[20:21], v[174:175] op_sel_hi:[1,0,0]
	s_waitcnt lgkmcnt(0)
	v_pk_add_f32 v[146:147], v[176:177], v[178:179]
	ds_bpermute_b32 v177, v192, v147
	ds_bpermute_b32 v176, v192, v146
	v_mul_f32_e32 v150, 0x4b800000, v145
	v_cmp_gt_f32_e64 s[0:1], s36, v145
	v_cmp_gt_f32_e64 s[2:3], s36, v144
	v_pk_add_f32 v[178:179], v[206:207], 1.0 op_sel_hi:[1,0]
	s_waitcnt lgkmcnt(0)
	v_pk_add_f32 v[146:147], v[146:147], v[176:177]
	ds_bpermute_b32 v177, v193, v147
	ds_bpermute_b32 v176, v193, v146
	v_cndmask_b32_e64 v145, v145, v150, s[0:1]
	v_rsq_f32_e32 v150, v145
	v_mul_f32_e32 v145, 0x4b800000, v144
	v_cndmask_b32_e64 v144, v144, v145, s[2:3]
	v_rsq_f32_e32 v161, v144
	s_waitcnt lgkmcnt(0)
	v_pk_add_f32 v[144:145], v[146:147], v[176:177]
	ds_bpermute_b32 v147, v194, v145
	ds_bpermute_b32 v146, v194, v144
	v_mul_f32_e32 v163, 0x45800000, v150
	v_cndmask_b32_e64 v180, v150, v163, s[0:1]
	v_mul_f32_e32 v150, 0x45800000, v161
	v_cndmask_b32_e64 v182, v161, v150, s[2:3]
	s_waitcnt lgkmcnt(0)
	v_pk_add_f32 v[144:145], v[144:145], v[146:147]
	v_pk_add_f32 v[176:177], v[208:209], 1.0 op_sel_hi:[1,0]
	v_pk_fma_f32 v[144:145], v[144:145], s[20:21], v[174:175] op_sel_hi:[1,0,0]
	s_waitcnt vmcnt(0)
	v_mov_b64_e32 v[202:203], v[240:241]
	v_mov_b64_e32 v[204:205], v[242:243]
	v_pk_mul_f32 v[204:205], v[204:205], v[176:177]
	v_mul_f32_e32 v146, 0x4b800000, v145
	v_cmp_gt_f32_e64 s[0:1], s36, v145
	v_cmp_gt_f32_e64 s[2:3], s36, v144
	v_pk_mul_f32 v[202:203], v[202:203], v[178:179]
	v_cndmask_b32_e64 v145, v145, v146, s[0:1]
	v_mul_f32_e32 v146, 0x4b800000, v144
	v_rsq_f32_e32 v145, v145
	v_cndmask_b32_e64 v144, v144, v146, s[2:3]
	v_rsq_f32_e32 v144, v144
	v_pk_mul_f32 v[132:133], v[132:133], v[182:183] op_sel_hi:[1,0]
	v_mul_f32_e32 v146, 0x45800000, v145
	v_cndmask_b32_e64 v184, v145, v146, s[0:1]
	v_mul_f32_e32 v145, 0x45800000, v144
	v_cndmask_b32_e64 v150, v144, v145, s[2:3]
	ds_read_b128 v[144:147], v196
	ds_read_b128 v[210:213], v196 offset:5120
	v_pk_mul_f32 v[134:135], v[134:135], v[182:183] op_sel_hi:[1,0]
	v_pk_mul_f32 v[206:207], v[128:129], v[180:181] op_sel_hi:[1,0]
	v_pk_mul_f32 v[208:209], v[130:131], v[180:181] op_sel_hi:[1,0]
	s_waitcnt lgkmcnt(1)
	v_pk_fma_f32 v[134:135], v[134:135], v[204:205], v[146:147]
	v_pk_fma_f32 v[132:133], v[132:133], v[202:203], v[144:145]
	v_pk_fma_f32 v[208:209], v[208:209], v[204:205], v[146:147]
	v_cvt_pk_bf16_f32 v132, v132, v133
	v_cvt_pk_bf16_f32 v133, v134, v135
	v_lshl_add_u64 v[134:135], v[158:159], 0, v[168:169]
	global_store_dwordx2 v[134:135], v[132:133], off
	v_pk_mul_f32 v[132:133], v[136:137], v[184:185] op_sel_hi:[1,0]
	v_pk_mul_f32 v[134:135], v[138:139], v[184:185] op_sel_hi:[1,0]
	v_pk_fma_f32 v[132:133], v[202:203], v[132:133], v[144:145]
	v_pk_fma_f32 v[134:135], v[204:205], v[134:135], v[146:147]
	v_cvt_pk_bf16_f32 v132, v132, v133
	v_cvt_pk_bf16_f32 v133, v134, v135
	v_lshl_add_u64 v[134:135], v[158:159], 0, v[170:171]
	v_pk_fma_f32 v[206:207], v[206:207], v[202:203], v[144:145]
	global_store_dwordx2 v[134:135], v[132:133], off
	v_pk_mul_f32 v[132:133], v[140:141], v[150:151] op_sel_hi:[1,0]
	v_pk_mul_f32 v[134:135], v[142:143], v[150:151] op_sel_hi:[1,0]
	v_cvt_pk_bf16_f32 v206, v206, v207
	v_cvt_pk_bf16_f32 v207, v208, v209
	v_lshlrev_b64 v[208:209], 11, v[166:167]
	v_pk_fma_f32 v[134:135], v[204:205], v[134:135], v[146:147]
	v_pk_fma_f32 v[132:133], v[202:203], v[132:133], v[144:145]
	v_lshlrev_b64 v[140:141], 11, v[172:173]
	v_lshl_add_u64 v[214:215], v[158:159], 0, v[208:209]
	v_cvt_pk_bf16_f32 v132, v132, v133
	v_cvt_pk_bf16_f32 v133, v134, v135
	v_lshl_add_u64 v[134:135], v[158:159], 0, v[140:141]
	global_store_dwordx2 v[214:215], v[206:207], off
	global_store_dwordx2 v[134:135], v[132:133], off
	v_mov_b64_e32 v[136:137], v[244:245]
	v_mov_b64_e32 v[138:139], v[246:247]
	ds_read_b128 v[128:131], v196 offset:1024
	s_waitcnt lgkmcnt(1)
	v_pk_add_f32 v[132:133], v[212:213], 1.0 op_sel_hi:[1,0]
	v_pk_add_f32 v[134:135], v[210:211], 1.0 op_sel_hi:[1,0]
	v_pk_mul_f32 v[124:125], v[124:125], v[180:181] op_sel_hi:[1,0]
	v_pk_mul_f32 v[126:127], v[126:127], v[180:181] op_sel_hi:[1,0]
	v_pk_mul_f32 v[112:113], v[112:113], v[182:183] op_sel_hi:[1,0]
	v_pk_mul_f32 v[114:115], v[114:115], v[182:183] op_sel_hi:[1,0]
	v_mov_b32_e32 v161, v151
	v_lshl_add_u64 v[172:173], s[16:17], 0, v[168:169]
	v_pk_mul_f32 v[100:101], v[100:101], v[182:183] op_sel_hi:[1,0]
	v_pk_mul_f32 v[102:103], v[102:103], v[182:183] op_sel_hi:[1,0]
	v_mov_b32_e32 v163, v151
	v_pk_mul_f32 v[84:85], v[84:85], v[180:181] op_sel_hi:[1,0]
	v_pk_mul_f32 v[86:87], v[86:87], v[180:181] op_sel_hi:[1,0]
	v_pk_mul_f32 v[88:89], v[88:89], v[182:183] op_sel_hi:[1,0]
	v_pk_mul_f32 v[90:91], v[90:91], v[182:183] op_sel_hi:[1,0]
	v_pk_mul_f32 v[80:81], v[80:81], v[150:151] op_sel_hi:[1,0]
	v_pk_mul_f32 v[82:83], v[82:83], v[150:151] op_sel_hi:[1,0]
	v_pk_mul_f32 v[92:93], v[92:93], v[184:185] op_sel_hi:[1,0]
	v_pk_mul_f32 v[94:95], v[94:95], v[184:185] op_sel_hi:[1,0]
	s_nop 0
	v_pk_mul_f32 v[138:139], v[138:139], v[132:133]
	v_pk_mul_f32 v[136:137], v[136:137], v[134:135]
	s_waitcnt lgkmcnt(0)
	v_pk_fma_f32 v[126:127], v[126:127], v[138:139], v[130:131]
	v_pk_fma_f32 v[124:125], v[124:125], v[136:137], v[128:129]
	v_pk_fma_f32 v[114:115], v[114:115], v[138:139], v[130:131]
	v_pk_fma_f32 v[112:113], v[112:113], v[136:137], v[128:129]
	v_cvt_pk_bf16_f32 v124, v124, v125
	v_cvt_pk_bf16_f32 v125, v126, v127
	v_lshl_add_u64 v[126:127], s[16:17], 0, v[208:209]
	v_cvt_pk_bf16_f32 v112, v112, v113
	v_cvt_pk_bf16_f32 v113, v114, v115
	v_lshl_add_u64 v[114:115], v[172:173], 0, v[160:161]
	v_lshl_add_u64 v[142:143], v[126:127], 0, v[160:161]
	global_store_dwordx2 v[114:115], v[112:113], off
	v_pk_mul_f32 v[112:113], v[116:117], v[184:185] op_sel_hi:[1,0]
	v_pk_mul_f32 v[114:115], v[118:119], v[184:185] op_sel_hi:[1,0]
	global_store_dwordx2 v[142:143], v[124:125], off
	v_pk_fma_f32 v[114:115], v[114:115], v[138:139], v[130:131]
	v_pk_fma_f32 v[112:113], v[112:113], v[136:137], v[128:129]
	v_lshl_add_u64 v[124:125], s[16:17], 0, v[170:171]
	v_cvt_pk_bf16_f32 v112, v112, v113
	v_cvt_pk_bf16_f32 v113, v114, v115
	v_lshl_add_u64 v[114:115], v[124:125], 0, v[160:161]
	global_store_dwordx2 v[114:115], v[112:113], off
	v_pk_mul_f32 v[112:113], v[120:121], v[150:151] op_sel_hi:[1,0]
	v_pk_mul_f32 v[114:115], v[122:123], v[150:151] op_sel_hi:[1,0]
	v_pk_fma_f32 v[112:113], v[136:137], v[112:113], v[128:129]
	v_pk_fma_f32 v[114:115], v[138:139], v[114:115], v[130:131]
	v_lshl_add_u64 v[120:121], s[16:17], 0, v[140:141]
	v_cvt_pk_bf16_f32 v112, v112, v113
	v_cvt_pk_bf16_f32 v113, v114, v115
	v_lshl_add_u64 v[114:115], v[120:121], 0, v[160:161]
	global_store_dwordx2 v[114:115], v[112:113], off
	v_mov_b64_e32 v[136:137], v[248:249]
	v_mov_b64_e32 v[138:139], v[250:251]
	ds_read_b128 v[140:143], v196 offset:6144
	ds_read_b128 v[112:115], v196 offset:2048
	ds_read_b128 v[168:171], v196 offset:7168
	s_waitcnt lgkmcnt(2)
	v_pk_add_f32 v[116:117], v[142:143], 1.0 op_sel_hi:[1,0]
	v_pk_add_f32 v[118:119], v[140:141], 1.0 op_sel_hi:[1,0]
	v_pk_mul_f32 v[140:141], v[98:99], v[180:181] op_sel_hi:[1,0]
	s_nop 0
	v_pk_mul_f32 v[122:123], v[138:139], v[116:117]
	v_pk_mul_f32 v[136:137], v[136:137], v[118:119]
	s_waitcnt lgkmcnt(1)
	v_pk_fma_f32 v[102:103], v[102:103], v[122:123], v[114:115]
	v_pk_fma_f32 v[100:101], v[100:101], v[136:137], v[112:113]
	v_pk_mul_f32 v[138:139], v[96:97], v[180:181] op_sel_hi:[1,0]
	v_cvt_pk_bf16_f32 v100, v100, v101
	v_cvt_pk_bf16_f32 v101, v102, v103
	v_lshl_add_u64 v[102:103], v[172:173], 0, v[162:163]
	global_store_dwordx2 v[102:103], v[100:101], off
	v_pk_mul_f32 v[100:101], v[104:105], v[184:185] op_sel_hi:[1,0]
	v_pk_mul_f32 v[102:103], v[106:107], v[184:185] op_sel_hi:[1,0]
	v_pk_fma_f32 v[100:101], v[100:101], v[136:137], v[112:113]
	v_pk_fma_f32 v[102:103], v[102:103], v[122:123], v[114:115]
	v_cvt_pk_bf16_f32 v100, v100, v101
	v_cvt_pk_bf16_f32 v101, v102, v103
	v_lshl_add_u64 v[102:103], v[124:125], 0, v[162:163]
	global_store_dwordx2 v[102:103], v[100:101], off
	v_pk_mul_f32 v[100:101], v[108:109], v[150:151] op_sel_hi:[1,0]
	v_pk_mul_f32 v[102:103], v[110:111], v[150:151] op_sel_hi:[1,0]
	v_pk_fma_f32 v[140:141], v[140:141], v[122:123], v[114:115]
	v_pk_fma_f32 v[138:139], v[138:139], v[136:137], v[112:113]
	v_pk_fma_f32 v[102:103], v[102:103], v[122:123], v[114:115]
	v_pk_fma_f32 v[100:101], v[100:101], v[136:137], v[112:113]
	v_cvt_pk_bf16_f32 v138, v138, v139
	v_cvt_pk_bf16_f32 v139, v140, v141
	v_lshl_add_u64 v[140:141], v[126:127], 0, v[162:163]
	v_cvt_pk_bf16_f32 v100, v100, v101
	v_cvt_pk_bf16_f32 v101, v102, v103
	v_lshl_add_u64 v[102:103], v[120:121], 0, v[162:163]
	global_store_dwordx2 v[140:141], v[138:139], off
	global_store_dwordx2 v[102:103], v[100:101], off
	v_mov_b64_e32 v[104:105], v[252:253]
	v_mov_b64_e32 v[106:107], v[254:255]
	ds_read_b128 v[96:99], v196 offset:3072
	s_waitcnt lgkmcnt(1)
	v_pk_add_f32 v[100:101], v[170:171], 1.0 op_sel_hi:[1,0]
	v_pk_add_f32 v[102:103], v[168:169], 1.0 op_sel_hi:[1,0]
	v_lshl_add_u64 v[110:111], v[126:127], 0, v[164:165]
	v_lshl_add_u64 v[122:123], v[172:173], 0, v[164:165]
	v_mov_b32_e32 v108, v76
	v_mov_b32_e32 v109, v60
	s_nop 0
	v_pk_mul_f32 v[106:107], v[106:107], v[100:101]
	v_pk_mul_f32 v[104:105], v[104:105], v[102:103]
	s_waitcnt lgkmcnt(0)
	v_pk_fma_f32 v[86:87], v[86:87], v[106:107], v[98:99]
	v_pk_fma_f32 v[84:85], v[84:85], v[104:105], v[96:97]
	v_pk_fma_f32 v[90:91], v[90:91], v[106:107], v[98:99]
	v_pk_fma_f32 v[88:89], v[88:89], v[104:105], v[96:97]
	v_cvt_pk_bf16_f32 v84, v84, v85
	v_cvt_pk_bf16_f32 v85, v86, v87
	v_cvt_pk_bf16_f32 v86, v88, v89
	v_cvt_pk_bf16_f32 v87, v90, v91
	global_store_dwordx2 v[110:111], v[84:85], off
	global_store_dwordx2 v[122:123], v[86:87], off
	v_mov_b32_e32 v84, v77
	v_mov_b32_e32 v85, v61
	v_pk_mul_f32 v[84:85], v[84:85], v[84:85]
	v_mov_b32_e32 v86, v78
	v_pk_fma_f32 v[84:85], v[108:109], v[108:109], v[84:85]
	v_mov_b32_e32 v87, v62
	v_pk_fma_f32 v[84:85], v[86:87], v[86:87], v[84:85]
	v_mov_b32_e32 v86, v79
	v_mov_b32_e32 v87, v63
	v_mov_b32_e32 v88, v45
	v_mov_b32_e32 v89, v21
	v_pk_fma_f32 v[84:85], v[86:87], v[86:87], v[84:85]
	v_mov_b32_e32 v86, v44
	v_mov_b32_e32 v87, v20
	v_pk_mul_f32 v[88:89], v[88:89], v[88:89]
	v_mov_b32_e32 v90, v73
	v_pk_fma_f32 v[86:87], v[86:87], v[86:87], v[88:89]
	v_mov_b32_e32 v88, v46
	v_mov_b32_e32 v89, v22
	v_pk_fma_f32 v[86:87], v[88:89], v[88:89], v[86:87]
	v_mov_b32_e32 v88, v47
	v_mov_b32_e32 v89, v23
	v_mov_b32_e32 v91, v57
	v_pk_fma_f32 v[86:87], v[88:89], v[88:89], v[86:87]
	v_mov_b32_e32 v88, v72
	v_mov_b32_e32 v89, v56
	v_pk_mul_f32 v[90:91], v[90:91], v[90:91]
	v_mov_b32_e32 v108, v41
	v_pk_fma_f32 v[88:89], v[88:89], v[88:89], v[90:91]
	v_mov_b32_e32 v90, v74
	v_mov_b32_e32 v91, v58
	v_pk_fma_f32 v[88:89], v[90:91], v[90:91], v[88:89]
	v_mov_b32_e32 v90, v75
	v_mov_b32_e32 v91, v59
	v_mov_b32_e32 v109, v25
	v_pk_fma_f32 v[88:89], v[90:91], v[90:91], v[88:89]
	v_mov_b32_e32 v90, v40
	v_mov_b32_e32 v91, v24
	v_pk_mul_f32 v[108:109], v[108:109], v[108:109]
	v_pk_fma_f32 v[82:83], v[82:83], v[106:107], v[98:99]
	v_pk_fma_f32 v[80:81], v[80:81], v[104:105], v[96:97]
	v_pk_fma_f32 v[90:91], v[90:91], v[90:91], v[108:109]
	v_mov_b32_e32 v108, v42
	v_mov_b32_e32 v109, v26
	v_cvt_pk_bf16_f32 v80, v80, v81
	v_cvt_pk_bf16_f32 v81, v82, v83
	v_lshl_add_u64 v[82:83], v[120:121], 0, v[164:165]
	v_pk_fma_f32 v[90:91], v[108:109], v[108:109], v[90:91]
	v_mov_b32_e32 v108, v43
	v_mov_b32_e32 v109, v27
	global_store_dwordx2 v[82:83], v[80:81], off
	v_mov_b32_e32 v82, v69
	v_mov_b32_e32 v83, v53
	v_pk_fma_f32 v[90:91], v[108:109], v[108:109], v[90:91]
	v_mov_b32_e32 v108, v88
	v_mov_b32_e32 v109, v84
	v_mov_b32_e32 v84, v89
	v_mov_b32_e32 v80, v68
	v_mov_b32_e32 v81, v52
	v_pk_mul_f32 v[82:83], v[82:83], v[82:83]
	v_pk_fma_f32 v[94:95], v[94:95], v[106:107], v[98:99]
	v_pk_fma_f32 v[92:93], v[92:93], v[104:105], v[96:97]
	v_pk_add_f32 v[84:85], v[108:109], v[84:85]
	v_mov_b32_e32 v88, v90
	v_mov_b32_e32 v89, v86
	v_pk_fma_f32 v[80:81], v[80:81], v[80:81], v[82:83]
	v_mov_b32_e32 v82, v70
	v_mov_b32_e32 v83, v54
	v_pk_add_f32 v[84:85], v[84:85], v[88:89]
	v_mov_b32_e32 v86, v91
	v_cvt_pk_bf16_f32 v88, v92, v93
	v_cvt_pk_bf16_f32 v89, v94, v95
	v_lshl_add_u64 v[90:91], v[124:125], 0, v[164:165]
	v_pk_fma_f32 v[80:81], v[82:83], v[82:83], v[80:81]
	v_mov_b32_e32 v82, v71
	v_mov_b32_e32 v83, v55
	global_store_dwordx2 v[90:91], v[88:89], off
	v_pk_fma_f32 v[88:89], v[82:83], v[82:83], v[80:81]
	v_mov_b32_e32 v82, v37
	v_mov_b32_e32 v83, v29
	v_mov_b32_e32 v80, v36
	v_mov_b32_e32 v81, v28
	v_pk_mul_f32 v[82:83], v[82:83], v[82:83]
	v_pk_add_f32 v[84:85], v[84:85], v[86:87]
	v_pk_fma_f32 v[80:81], v[80:81], v[80:81], v[82:83]
	v_mov_b32_e32 v82, v38
	v_mov_b32_e32 v83, v30
	v_pk_fma_f32 v[80:81], v[82:83], v[82:83], v[80:81]
	v_mov_b32_e32 v82, v39
	v_mov_b32_e32 v83, v31
	v_pk_fma_f32 v[90:91], v[82:83], v[82:83], v[80:81]
	v_mov_b32_e32 v82, v65
	v_mov_b32_e32 v83, v49
	v_mov_b32_e32 v80, v64
	v_mov_b32_e32 v81, v48
	v_pk_mul_f32 v[82:83], v[82:83], v[82:83]
	ds_bpermute_b32 v87, v189, v85
	v_pk_fma_f32 v[80:81], v[80:81], v[80:81], v[82:83]
	v_mov_b32_e32 v82, v66
	v_mov_b32_e32 v83, v50
	v_pk_fma_f32 v[92:93], v[82:83], v[82:83], v[80:81]
	v_mov_b64_e32 v[80:81], v[240:241]
	v_mov_b64_e32 v[82:83], v[242:243]
	ds_bpermute_b32 v86, v189, v84
	v_mov_b32_e32 v94, v67
	v_mov_b32_e32 v95, v51
	v_mov_b32_e32 v104, v33
	v_mov_b32_e32 v105, v17
	s_waitcnt lgkmcnt(0)
	v_pk_add_f32 v[84:85], v[84:85], v[86:87]
	ds_bpermute_b32 v87, v190, v85
	ds_bpermute_b32 v86, v190, v84
	v_pk_fma_f32 v[92:93], v[94:95], v[94:95], v[92:93]
	v_mov_b32_e32 v94, v32
	v_mov_b32_e32 v95, v16
	v_pk_mul_f32 v[104:105], v[104:105], v[104:105]
	s_waitcnt lgkmcnt(0)
	v_pk_add_f32 v[84:85], v[84:85], v[86:87]
	ds_bpermute_b32 v87, v191, v85
	ds_bpermute_b32 v86, v191, v84
	v_pk_fma_f32 v[94:95], v[94:95], v[94:95], v[104:105]
	v_mov_b32_e32 v104, v34
	v_mov_b32_e32 v105, v18
	v_pk_fma_f32 v[94:95], v[104:105], v[104:105], v[94:95]
	v_mov_b32_e32 v104, v35
	v_mov_b32_e32 v105, v19
	v_pk_fma_f32 v[94:95], v[104:105], v[104:105], v[94:95]
	v_mov_b32_e32 v104, v92
	v_mov_b32_e32 v105, v88
	v_mov_b32_e32 v88, v93
	v_pk_add_f32 v[88:89], v[104:105], v[88:89]
	v_mov_b32_e32 v92, v94
	v_mov_b32_e32 v93, v90
	v_pk_add_f32 v[88:89], v[88:89], v[92:93]
	v_mov_b32_e32 v90, v95
	s_waitcnt lgkmcnt(0)
	v_pk_add_f32 v[84:85], v[84:85], v[86:87]
	v_pk_add_f32 v[88:89], v[88:89], v[90:91]
	ds_bpermute_b32 v87, v192, v85
	ds_bpermute_b32 v86, v192, v84
	ds_bpermute_b32 v91, v189, v89
	ds_bpermute_b32 v90, v189, v88
	v_or_b32_e32 v92, 4, v166
	v_ashrrev_i32_e32 v93, 31, v92
	s_waitcnt lgkmcnt(2)
	v_pk_add_f32 v[84:85], v[84:85], v[86:87]
	ds_bpermute_b32 v87, v193, v85
	s_waitcnt lgkmcnt(1)
	v_pk_add_f32 v[88:89], v[88:89], v[90:91]
	ds_bpermute_b32 v86, v193, v84
	ds_bpermute_b32 v91, v190, v89
	ds_bpermute_b32 v90, v190, v88
	s_waitcnt lgkmcnt(2)
	v_pk_add_f32 v[84:85], v[84:85], v[86:87]
	ds_bpermute_b32 v87, v194, v85
	s_waitcnt lgkmcnt(1)
	v_pk_add_f32 v[88:89], v[88:89], v[90:91]
	ds_bpermute_b32 v86, v194, v84
	ds_bpermute_b32 v91, v191, v89
	ds_bpermute_b32 v90, v191, v88
	s_waitcnt lgkmcnt(2)
	v_pk_add_f32 v[84:85], v[84:85], v[86:87]
	s_nop 0
	v_pk_fma_f32 v[84:85], v[84:85], s[20:21], v[174:175] op_sel_hi:[1,0,0]
	s_waitcnt lgkmcnt(0)
	v_pk_add_f32 v[86:87], v[88:89], v[90:91]
	ds_bpermute_b32 v89, v192, v87
	ds_bpermute_b32 v88, v192, v86
	v_mul_f32_e32 v90, 0x4b800000, v85
	v_cmp_gt_f32_e64 s[0:1], s36, v85
	v_cmp_gt_f32_e64 s[2:3], s36, v84
	s_waitcnt lgkmcnt(0)
	v_pk_add_f32 v[86:87], v[86:87], v[88:89]
	ds_bpermute_b32 v89, v193, v87
	ds_bpermute_b32 v88, v193, v86
	v_cndmask_b32_e64 v85, v85, v90, s[0:1]
	v_rsq_f32_e32 v90, v85
	v_mul_f32_e32 v85, 0x4b800000, v84
	v_cndmask_b32_e64 v84, v84, v85, s[2:3]
	v_rsq_f32_e32 v91, v84
	s_waitcnt lgkmcnt(0)
	v_pk_add_f32 v[84:85], v[86:87], v[88:89]
	ds_bpermute_b32 v87, v194, v85
	ds_bpermute_b32 v86, v194, v84
	v_mul_f32_e32 v88, 0x45800000, v90
	v_cndmask_b32_e64 v88, v90, v88, s[0:1]
	v_mul_f32_e32 v89, 0x45800000, v91
	v_pk_mul_f32 v[76:77], v[76:77], v[88:89] op_sel_hi:[1,0]
	s_waitcnt lgkmcnt(0)
	v_pk_add_f32 v[84:85], v[84:85], v[86:87]
	s_nop 0
	v_pk_mul_f32 v[82:83], v[176:177], v[82:83]
	v_pk_fma_f32 v[84:85], v[84:85], s[20:21], v[174:175] op_sel_hi:[1,0,0]
	v_pk_mul_f32 v[80:81], v[178:179], v[80:81]
	v_mul_f32_e32 v86, 0x4b800000, v85
	v_cmp_gt_f32_e64 s[0:1], s36, v85
	v_cmp_gt_f32_e64 s[4:5], s36, v84
	v_pk_mul_f32 v[78:79], v[78:79], v[88:89] op_sel_hi:[1,0]
	v_cndmask_b32_e64 v85, v85, v86, s[0:1]
	v_mul_f32_e32 v86, 0x4b800000, v84
	v_rsq_f32_e32 v85, v85
	v_cndmask_b32_e64 v84, v84, v86, s[4:5]
	v_rsq_f32_e32 v87, v84
	v_pk_fma_f32 v[78:79], v[78:79], v[82:83], v[146:147]
	v_pk_fma_f32 v[76:77], v[76:77], v[80:81], v[144:145]
	v_mul_f32_e32 v86, 0x45800000, v85
	v_cvt_pk_bf16_f32 v76, v76, v77
	v_cvt_pk_bf16_f32 v77, v78, v79
	v_lshlrev_b64 v[78:79], 11, v[92:93]
	v_cndmask_b32_e64 v84, v91, v89, s[2:3]
	v_cndmask_b32_e64 v86, v85, v86, s[0:1]
	v_mul_f32_e32 v85, 0x45800000, v87
	v_lshl_add_u64 v[92:93], v[158:159], 0, v[78:79]
	global_store_dwordx2 v[92:93], v[76:77], off
	v_or_b32_e32 v76, 5, v166
	v_pk_mul_f32 v[72:73], v[72:73], v[84:85] op_sel_hi:[1,0]
	v_pk_mul_f32 v[74:75], v[74:75], v[84:85] op_sel_hi:[1,0]
	v_pk_fma_f32 v[72:73], v[72:73], v[80:81], v[144:145]
	v_pk_fma_f32 v[74:75], v[74:75], v[82:83], v[146:147]
	v_ashrrev_i32_e32 v77, 31, v76
	v_cvt_pk_bf16_f32 v72, v72, v73
	v_cvt_pk_bf16_f32 v73, v74, v75
	v_lshlrev_b64 v[74:75], 11, v[76:77]
	v_lshl_add_u64 v[76:77], v[158:159], 0, v[74:75]
	global_store_dwordx2 v[76:77], v[72:73], off
	v_or_b32_e32 v72, 6, v166
	v_pk_mul_f32 v[68:69], v[68:69], v[86:87] op_sel_hi:[1,0]
	v_pk_mul_f32 v[70:71], v[70:71], v[86:87] op_sel_hi:[1,0]
	v_pk_fma_f32 v[68:69], v[80:81], v[68:69], v[144:145]
	v_pk_fma_f32 v[70:71], v[82:83], v[70:71], v[146:147]
	v_ashrrev_i32_e32 v73, 31, v72
	v_cvt_pk_bf16_f32 v68, v68, v69
	v_cvt_pk_bf16_f32 v69, v70, v71
	v_lshlrev_b64 v[70:71], 11, v[72:73]
	v_lshl_add_u64 v[72:73], v[158:159], 0, v[70:71]
	v_cndmask_b32_e64 v90, v87, v85, s[4:5]
	global_store_dwordx2 v[72:73], v[68:69], off
	v_or_b32_e32 v68, 7, v166
	v_pk_mul_f32 v[64:65], v[64:65], v[90:91] op_sel_hi:[1,0]
	v_pk_mul_f32 v[66:67], v[66:67], v[90:91] op_sel_hi:[1,0]
	v_ashrrev_i32_e32 v69, 31, v68
	v_pk_fma_f32 v[66:67], v[82:83], v[66:67], v[146:147]
	v_pk_fma_f32 v[64:65], v[80:81], v[64:65], v[144:145]
	v_lshlrev_b64 v[68:69], 11, v[68:69]
	v_cvt_pk_bf16_f32 v64, v64, v65
	v_cvt_pk_bf16_f32 v65, v66, v67
	v_lshl_add_u64 v[66:67], v[158:159], 0, v[68:69]
	global_store_dwordx2 v[66:67], v[64:65], off
	v_mov_b64_e32 v[64:65], v[244:245]
	v_mov_b64_e32 v[66:67], v[246:247]
	v_pk_mul_f32 v[60:61], v[60:61], v[88:89] op_sel_hi:[1,0]
	v_pk_mul_f32 v[62:63], v[62:63], v[88:89] op_sel_hi:[1,0]
	v_pk_mul_f32 v[56:57], v[56:57], v[84:85] op_sel_hi:[1,0]
	v_pk_mul_f32 v[58:59], v[58:59], v[84:85] op_sel_hi:[1,0]
	v_pk_mul_f32 v[52:53], v[52:53], v[86:87] op_sel_hi:[1,0]
	v_pk_mul_f32 v[54:55], v[54:55], v[86:87] op_sel_hi:[1,0]
	v_pk_mul_f32 v[48:49], v[48:49], v[90:91] op_sel_hi:[1,0]
	v_pk_mul_f32 v[50:51], v[50:51], v[90:91] op_sel_hi:[1,0]
	v_pk_mul_f32 v[44:45], v[44:45], v[88:89] op_sel_hi:[1,0]
	v_pk_mul_f32 v[46:47], v[46:47], v[88:89] op_sel_hi:[1,0]
	v_pk_mul_f32 v[40:41], v[40:41], v[84:85] op_sel_hi:[1,0]
	v_pk_mul_f32 v[42:43], v[42:43], v[84:85] op_sel_hi:[1,0]
	v_pk_mul_f32 v[36:37], v[36:37], v[86:87] op_sel_hi:[1,0]
	v_pk_mul_f32 v[38:39], v[38:39], v[86:87] op_sel_hi:[1,0]
	v_pk_mul_f32 v[32:33], v[32:33], v[90:91] op_sel_hi:[1,0]
	v_pk_mul_f32 v[34:35], v[34:35], v[90:91] op_sel_hi:[1,0]
	v_pk_mul_f32 v[20:21], v[20:21], v[88:89] op_sel_hi:[1,0]
	v_pk_mul_f32 v[22:23], v[22:23], v[88:89] op_sel_hi:[1,0]
	v_pk_mul_f32 v[16:17], v[16:17], v[90:91] op_sel_hi:[1,0]
	v_pk_mul_f32 v[18:19], v[18:19], v[90:91] op_sel_hi:[1,0]
	v_pk_mul_f32 v[24:25], v[24:25], v[84:85] op_sel_hi:[1,0]
	v_pk_mul_f32 v[26:27], v[26:27], v[84:85] op_sel_hi:[1,0]
	v_pk_mul_f32 v[28:29], v[28:29], v[86:87] op_sel_hi:[1,0]
	v_pk_mul_f32 v[30:31], v[30:31], v[86:87] op_sel_hi:[1,0]
	s_nop 0
	v_pk_mul_f32 v[66:67], v[132:133], v[66:67]
	v_pk_mul_f32 v[64:65], v[134:135], v[64:65]
	v_pk_fma_f32 v[62:63], v[62:63], v[66:67], v[130:131]
	v_pk_fma_f32 v[60:61], v[60:61], v[64:65], v[128:129]
	v_pk_fma_f32 v[58:59], v[58:59], v[66:67], v[130:131]
	v_cvt_pk_bf16_f32 v60, v60, v61
	v_cvt_pk_bf16_f32 v61, v62, v63
	v_lshl_add_u64 v[62:63], s[16:17], 0, v[78:79]
	v_pk_fma_f32 v[56:57], v[56:57], v[64:65], v[128:129]
	v_lshl_add_u64 v[72:73], v[62:63], 0, v[160:161]
	v_cvt_pk_bf16_f32 v56, v56, v57
	v_cvt_pk_bf16_f32 v57, v58, v59
	v_lshl_add_u64 v[58:59], s[16:17], 0, v[74:75]
	v_pk_fma_f32 v[54:55], v[54:55], v[66:67], v[130:131]
	v_pk_fma_f32 v[52:53], v[52:53], v[64:65], v[128:129]
	global_store_dwordx2 v[72:73], v[60:61], off
	v_lshl_add_u64 v[60:61], v[58:59], 0, v[160:161]
	v_cvt_pk_bf16_f32 v52, v52, v53
	v_cvt_pk_bf16_f32 v53, v54, v55
	v_lshl_add_u64 v[54:55], s[16:17], 0, v[70:71]
	global_store_dwordx2 v[60:61], v[56:57], off
	v_lshl_add_u64 v[56:57], v[54:55], 0, v[160:161]
	global_store_dwordx2 v[56:57], v[52:53], off
	v_pk_fma_f32 v[50:51], v[66:67], v[50:51], v[130:131]
	v_pk_fma_f32 v[48:49], v[64:65], v[48:49], v[128:129]
	v_lshl_add_u64 v[52:53], s[16:17], 0, v[68:69]
	v_cvt_pk_bf16_f32 v48, v48, v49
	v_cvt_pk_bf16_f32 v49, v50, v51
	v_lshl_add_u64 v[50:51], v[52:53], 0, v[160:161]
	global_store_dwordx2 v[50:51], v[48:49], off
	v_mov_b64_e32 v[48:49], v[248:249]
	v_mov_b64_e32 v[50:51], v[250:251]
	s_nop 0
	v_pk_mul_f32 v[50:51], v[116:117], v[50:51]
	v_pk_mul_f32 v[48:49], v[118:119], v[48:49]
	v_pk_fma_f32 v[46:47], v[46:47], v[50:51], v[114:115]
	v_pk_fma_f32 v[44:45], v[44:45], v[48:49], v[112:113]
	v_pk_fma_f32 v[42:43], v[42:43], v[50:51], v[114:115]
	v_pk_fma_f32 v[40:41], v[40:41], v[48:49], v[112:113]
	v_pk_fma_f32 v[38:39], v[38:39], v[50:51], v[114:115]
	v_pk_fma_f32 v[36:37], v[36:37], v[48:49], v[112:113]
	v_pk_fma_f32 v[34:35], v[50:51], v[34:35], v[114:115]
	v_pk_fma_f32 v[32:33], v[48:49], v[32:33], v[112:113]
	v_cvt_pk_bf16_f32 v44, v44, v45
	v_cvt_pk_bf16_f32 v45, v46, v47
	v_lshl_add_u64 v[46:47], v[62:63], 0, v[162:163]
	v_cvt_pk_bf16_f32 v40, v40, v41
	v_cvt_pk_bf16_f32 v41, v42, v43
	v_lshl_add_u64 v[42:43], v[58:59], 0, v[162:163]
	v_cvt_pk_bf16_f32 v36, v36, v37
	v_cvt_pk_bf16_f32 v37, v38, v39
	v_lshl_add_u64 v[38:39], v[54:55], 0, v[162:163]
	v_cvt_pk_bf16_f32 v32, v32, v33
	v_cvt_pk_bf16_f32 v33, v34, v35
	v_lshl_add_u64 v[34:35], v[52:53], 0, v[162:163]
	global_store_dwordx2 v[46:47], v[44:45], off
	global_store_dwordx2 v[42:43], v[40:41], off
	global_store_dwordx2 v[38:39], v[36:37], off
	global_store_dwordx2 v[34:35], v[32:33], off
	v_mov_b64_e32 v[32:33], v[252:253]
	v_mov_b64_e32 v[34:35], v[254:255]
	v_lshl_add_u64 v[36:37], v[62:63], 0, v[164:165]
	v_lshl_add_u64 v[38:39], v[58:59], 0, v[164:165]
	v_lshl_add_u64 v[40:41], v[54:55], 0, v[164:165]
	s_nop 0
	v_pk_mul_f32 v[34:35], v[100:101], v[34:35]
	v_pk_mul_f32 v[32:33], v[102:103], v[32:33]
	v_pk_fma_f32 v[22:23], v[22:23], v[34:35], v[98:99]
	v_pk_fma_f32 v[20:21], v[20:21], v[32:33], v[96:97]
	v_pk_fma_f32 v[18:19], v[18:19], v[34:35], v[98:99]
	v_pk_fma_f32 v[16:17], v[16:17], v[32:33], v[96:97]
	v_pk_fma_f32 v[26:27], v[26:27], v[34:35], v[98:99]
	v_pk_fma_f32 v[24:25], v[24:25], v[32:33], v[96:97]
	v_pk_fma_f32 v[30:31], v[30:31], v[34:35], v[98:99]
	v_pk_fma_f32 v[28:29], v[28:29], v[32:33], v[96:97]
	v_cvt_pk_bf16_f32 v20, v20, v21
	v_cvt_pk_bf16_f32 v21, v22, v23
	v_cvt_pk_bf16_f32 v16, v16, v17
	v_cvt_pk_bf16_f32 v17, v18, v19
	v_lshl_add_u64 v[18:19], v[52:53], 0, v[164:165]
	v_cvt_pk_bf16_f32 v22, v24, v25
	v_cvt_pk_bf16_f32 v23, v26, v27
	v_cvt_pk_bf16_f32 v24, v28, v29
	v_cvt_pk_bf16_f32 v25, v30, v31
	global_store_dwordx2 v[36:37], v[20:21], off
	global_store_dwordx2 v[38:39], v[22:23], off
	global_store_dwordx2 v[40:41], v[24:25], off
	global_store_dwordx2 v[18:19], v[16:17], off
	s_and_saveexec_b64 s[2:3], s[8:9]
	s_cbranch_execz .LBB0_142
	v_mov_b64_e32 v[16:17], v[240:241]
	v_mov_b64_e32 v[18:19], v[242:243]
	v_mov_b32_e32 v22, v13
	v_mov_b32_e32 v23, v9
	v_mov_b32_e32 v20, v12
	v_mov_b32_e32 v21, v8
	v_mov_b32_e32 v30, v5
	v_mov_b32_e32 v31, v1
	v_pk_mul_f32 v[22:23], v[22:23], v[22:23]
	v_mov_b32_e32 v24, v14
	v_mov_b32_e32 v25, v10
	v_mov_b32_e32 v28, v4
	v_mov_b32_e32 v29, v0
	v_pk_mul_f32 v[30:31], v[30:31], v[30:31]
	v_pk_fma_f32 v[20:21], v[20:21], v[20:21], v[22:23]
	v_mov_b32_e32 v26, v15
	v_mov_b32_e32 v27, v11
	v_mov_b32_e32 v32, v6
	v_mov_b32_e32 v33, v2
	v_pk_fma_f32 v[22:23], v[28:29], v[28:29], v[30:31]
	v_pk_fma_f32 v[20:21], v[24:25], v[24:25], v[20:21]
	v_mov_b32_e32 v34, v7
	v_mov_b32_e32 v35, v3
	v_pk_fma_f32 v[22:23], v[32:33], v[32:33], v[22:23]
	v_pk_fma_f32 v[20:21], v[26:27], v[26:27], v[20:21]
	v_pk_fma_f32 v[22:23], v[34:35], v[34:35], v[22:23]
	v_add_f32_e32 v20, v20, v21
	v_add_f32_e32 v20, v20, v22
	v_add_f32_e32 v20, v20, v23
	ds_bpermute_b32 v21, v189, v20
	v_add_u32_e32 v36, s38, v195
	v_ashrrev_i32_e32 v37, 31, v36
	v_lshlrev_b64 v[36:37], 11, v[36:37]
	v_lshl_add_u64 v[36:37], v[158:159], 0, v[36:37]
	s_waitcnt lgkmcnt(0)
	v_add_f32_e32 v20, v20, v21
	ds_bpermute_b32 v21, v190, v20
	s_waitcnt lgkmcnt(0)
	v_add_f32_e32 v20, v20, v21
	ds_bpermute_b32 v21, v191, v20
	s_waitcnt lgkmcnt(0)
	v_add_f32_e32 v20, v20, v21
	ds_bpermute_b32 v21, v192, v20
	s_waitcnt lgkmcnt(0)
	v_add_f32_e32 v28, v20, v21
	ds_bpermute_b32 v29, v193, v28
	ds_read_b128 v[20:23], v196 offset:8192
	ds_read_b128 v[24:27], v196 offset:9216
	s_waitcnt lgkmcnt(2)
	v_add_f32_e32 v38, v28, v29
	ds_bpermute_b32 v39, v194, v38
	ds_read_b128 v[28:31], v196 offset:12288
	ds_read_b128 v[32:35], v196 offset:13312
	s_waitcnt lgkmcnt(2)
	v_add_f32_e32 v38, v38, v39
	v_fmamk_f32 v38, v38, 0x3a800000, v200
	v_mul_f32_e32 v39, 0x4b800000, v38
	v_cmp_gt_f32_e64 s[0:1], s36, v38
	s_waitcnt lgkmcnt(1)
	v_pk_add_f32 v[30:31], v[30:31], 1.0 op_sel_hi:[1,0]
	v_pk_add_f32 v[28:29], v[28:29], 1.0 op_sel_hi:[1,0]
	v_cndmask_b32_e64 v38, v38, v39, s[0:1]
	v_rsq_f32_e32 v38, v38
	s_nop 0
	v_pk_mul_f32 v[18:19], v[18:19], v[30:31]
	v_mul_f32_e32 v39, 0x45800000, v38
	v_cndmask_b32_e64 v38, v38, v39, s[0:1]
	v_pk_mul_f32 v[12:13], v[12:13], v[38:39] op_sel_hi:[1,0]
	v_pk_mul_f32 v[14:15], v[14:15], v[38:39] op_sel_hi:[1,0]
	v_pk_mul_f32 v[16:17], v[16:17], v[28:29]
	v_pk_fma_f32 v[14:15], v[18:19], v[14:15], v[22:23]
	v_pk_fma_f32 v[12:13], v[16:17], v[12:13], v[20:21]
	s_waitcnt lgkmcnt(0)
	v_pk_add_f32 v[16:17], v[34:35], 1.0 op_sel_hi:[1,0]
	v_cvt_pk_bf16_f32 v12, v12, v13
	v_cvt_pk_bf16_f32 v13, v14, v15
	global_store_dwordx2 v[36:37], v[12:13], off
	v_mov_b64_e32 v[12:13], v[244:245]
	v_mov_b64_e32 v[14:15], v[246:247]
	v_pk_add_f32 v[18:19], v[32:33], 1.0 op_sel_hi:[1,0]
	v_pk_mul_f32 v[8:9], v[8:9], v[38:39] op_sel_hi:[1,0]
	v_pk_mul_f32 v[10:11], v[10:11], v[38:39] op_sel_hi:[1,0]
	v_pk_mul_f32 v[4:5], v[4:5], v[38:39] op_sel_hi:[1,0]
	v_pk_mul_f32 v[6:7], v[6:7], v[38:39] op_sel_hi:[1,0]
	v_pk_mul_f32 v[0:1], v[0:1], v[38:39] op_sel_hi:[1,0]
	v_pk_mul_f32 v[2:3], v[2:3], v[38:39] op_sel_hi:[1,0]
	s_nop 0
	v_pk_mul_f32 v[14:15], v[14:15], v[16:17]
	v_pk_mul_f32 v[12:13], v[12:13], v[18:19]
	v_pk_fma_f32 v[10:11], v[14:15], v[10:11], v[26:27]
	v_pk_fma_f32 v[8:9], v[12:13], v[8:9], v[24:25]
	s_nop 0
	v_cvt_pk_bf16_f32 v8, v8, v9
	v_cvt_pk_bf16_f32 v9, v10, v11
	global_store_dwordx2 v[36:37], v[8:9], off offset:512
	v_mov_b64_e32 v[8:9], v[248:249]
	v_mov_b64_e32 v[10:11], v[250:251]
	ds_read_b128 v[12:15], v196 offset:14336
	ds_read_b128 v[16:19], v196 offset:10240
	ds_read_b128 v[20:23], v196 offset:11264
	ds_read_b128 v[24:27], v196 offset:15360
	s_waitcnt lgkmcnt(3)
	v_pk_add_f32 v[14:15], v[14:15], 1.0 op_sel_hi:[1,0]
	v_pk_add_f32 v[12:13], v[12:13], 1.0 op_sel_hi:[1,0]
	s_nop 0
	v_pk_mul_f32 v[10:11], v[10:11], v[14:15]
	v_pk_mul_f32 v[8:9], v[8:9], v[12:13]
	s_waitcnt lgkmcnt(2)
	v_pk_fma_f32 v[6:7], v[6:7], v[10:11], v[18:19]
	v_pk_fma_f32 v[4:5], v[4:5], v[8:9], v[16:17]
	s_waitcnt lgkmcnt(0)
	v_pk_add_f32 v[8:9], v[26:27], 1.0 op_sel_hi:[1,0]
	v_cvt_pk_bf16_f32 v4, v4, v5
	v_cvt_pk_bf16_f32 v5, v6, v7
	global_store_dwordx2 v[36:37], v[4:5], off offset:1024
	v_mov_b64_e32 v[4:5], v[252:253]
	v_mov_b64_e32 v[6:7], v[254:255]
	v_pk_add_f32 v[10:11], v[24:25], 1.0 op_sel_hi:[1,0]
	s_nop 0
	v_pk_mul_f32 v[6:7], v[6:7], v[8:9]
	v_pk_mul_f32 v[4:5], v[4:5], v[10:11]
	v_pk_fma_f32 v[2:3], v[2:3], v[6:7], v[22:23]
	v_pk_fma_f32 v[0:1], v[0:1], v[4:5], v[20:21]
	s_nop 0
	v_cvt_pk_bf16_f32 v0, v0, v1
	v_cvt_pk_bf16_f32 v1, v2, v3
	global_store_dwordx2 v[36:37], v[0:1], off offset:1536
	s_branch .LBB0_142
